# XCD-aware placement for the RWKV scan: the two workgroups that scan the same unit now have equal blockIdx%8 (same XCD L2), so the shared 8 KB-per-chunk operator stream is fetched into one L2
# speedup vs baseline: 1.0041x; 1.0041x over previous
.LBB0_1299:
	s_or_b64 exec, exec, s[0:1]
	v_readlane_b32 s0, v232, 43
	s_ashr_i32 s15, s0, 6
	s_and_b32 s0, s15, 3
	s_waitcnt vmcnt(0)
	v_and_b32_e32 v1, 63, v70
	s_cmp_gt_u32 s0, 1
	s_waitcnt lgkmcnt(0)
	s_barrier
	s_cbranch_scc1 .Lcv0_idle
	s_lshr_b32 s1, s96, 2
	s_and_b32 s1, s1, 2
	s_lshr_b32 s14, s96, 1
	s_and_b32 s14, s14, 0x38
	s_and_b32 s13, s96, 7
	s_or_b32 s14, s14, s13
	s_or_b32 s13, s0, s1
	s_lshl_b32 s1, s0, 14
	s_and_b32 s16, s14, 1
	s_add_i32 s17, s1, 0
	s_lshl_b32 s12, s0, 6
	s_mov_b32 s18, 0
	s_mov_b64 s[6:7], -1
	s_cmp_gt_i32 s15, 3
	v_cmp_eq_u32_e64 s[0:1], 0, v1
	s_cbranch_scc1 .LBB0_1345
	s_setprio 3
	s_lshl_b32 s19, s14, 7
	s_cmp_eq_u32 s16, 0
	s_cselect_b64 s[6:7], -1, 0
	s_and_b64 s[8:9], s[6:7], exec
	s_cselect_b32 s2, 0, 0x7f
	s_cselect_b32 s3, 1, 0x7e
	s_or_b32 s22, s2, s19
	s_add_u32 s20, s4, 0x4400000
	s_addc_u32 s21, s5, 0
	s_ashr_i32 s23, s22, 31
	s_lshl_b64 s[10:11], s[22:23], 13
	s_add_u32 s24, s20, s10
	s_addc_u32 s25, s21, s11
	s_add_u32 s8, s4, 0x8400000
	s_addc_u32 s9, s5, 0
	s_add_u32 s26, s8, s10
	s_addc_u32 s27, s9, s11
	s_add_u32 s10, s4, 0x3ea00000
	v_mov_b32_e32 v175, 0
	s_addc_u32 s11, s5, 0
	s_lshl_b64 s[22:23], s[22:23], 8
	v_lshlrev_b32_e32 v54, 4, v1
	v_mov_b32_e32 v55, v175
	s_add_u32 s28, s10, s22
	v_lshlrev_b32_e32 v176, 3, v1
	v_lshl_add_u64 v[6:7], s[24:25], 0, v[54:55]
	s_movk_i32 s22, 0x1000
	v_or_b32_e32 v100, 0x800, v176
	v_add_co_u32_e32 v10, vcc, s22, v6
	v_or_b32_e32 v102, 0xc00, v176
	v_lshl_or_b32 v98, s13, 11, v176
	v_lshlrev_b32_e32 v56, 1, v100
	v_addc_co_u32_e32 v11, vcc, 0, v7, vcc
	v_lshlrev_b32_e32 v64, 1, v102
	s_addc_u32 s29, s11, s23
	v_and_b32_e32 v174, 48, v70
	global_load_dwordx4 v[38:41], v54, s[24:25]
	global_load_dwordx4 v[30:33], v54, s[24:25] offset:1024
	global_load_dwordx2 v[188:189], v98, s[26:27]
	global_load_dwordx4 v[46:49], v174, s[28:29]
	global_load_dwordx4 v[18:21], v54, s[24:25] offset:2048
	global_load_dwordx4 v[22:25], v54, s[24:25] offset:3072
	global_load_dwordx2 v[186:187], v98, s[26:27] offset:512
	global_load_dwordx4 v[42:45], v174, s[28:29] offset:64
	global_load_dwordx4 v[2:5], v56, s[24:25]
	global_load_dwordx4 v[14:17], v[10:11], off offset:1024
	global_load_dwordx2 v[182:183], v98, s[26:27] offset:1024
	global_load_dwordx4 v[26:29], v174, s[28:29] offset:128
	global_load_dwordx4 v[6:9], v64, s[24:25]
	s_nop 0
	global_load_dwordx4 v[10:13], v[10:11], off offset:3072
	s_nop 0
	global_load_dwordx2 v[184:185], v98, s[26:27] offset:1536
	global_load_dwordx4 v[34:37], v174, s[28:29] offset:192
	s_or_b32 s24, s3, s19
	s_ashr_i32 s25, s24, 31
	s_lshl_b64 s[26:27], s[24:25], 13
	s_add_u32 s28, s20, s26
	s_addc_u32 s29, s21, s27
	s_add_u32 s26, s8, s26
	s_addc_u32 s27, s9, s27
	s_lshl_b64 s[24:25], s[24:25], 8
	s_add_u32 s24, s10, s24
	v_lshl_add_u64 v[62:63], s[28:29], 0, v[54:55]
	s_addc_u32 s25, s11, s25
	global_load_dwordx4 v[78:81], v54, s[28:29]
	global_load_dwordx4 v[70:73], v54, s[28:29] offset:1024
	global_load_dwordx2 v[196:197], v98, s[26:27]
	global_load_dwordx4 v[94:97], v174, s[24:25]
	global_load_dwordx4 v[50:53], v54, s[28:29] offset:2048
	global_load_dwordx4 v[58:61], v54, s[28:29] offset:3072
	global_load_dwordx2 v[194:195], v98, s[26:27] offset:512
	global_load_dwordx4 v[82:85], v174, s[24:25] offset:64
	s_nop 0
	global_load_dwordx4 v[54:57], v56, s[28:29]
	v_add_co_u32_e32 v66, vcc, s22, v62
	v_mov_b32_e32 v99, v175
	s_nop 0
	v_addc_co_u32_e32 v67, vcc, 0, v63, vcc
	global_load_dwordx4 v[74:77], v[66:67], off offset:1024
	global_load_dwordx2 v[190:191], v98, s[26:27] offset:1024
	global_load_dwordx4 v[86:89], v174, s[24:25] offset:128
	s_nop 0
	global_load_dwordx4 v[62:65], v64, s[28:29]
	s_nop 0
	global_load_dwordx4 v[66:69], v[66:67], off offset:3072
	s_nop 0
	global_load_dwordx2 v[192:193], v98, s[26:27] offset:1536
	global_load_dwordx4 v[90:93], v174, s[24:25] offset:192
	v_lshl_add_u64 v[178:179], s[10:11], 0, v[174:175]
	v_lshl_add_u64 v[180:181], s[8:9], 0, v[98:99]
	v_add_u32_e32 v177, s17, v176
	v_lshlrev_b32_e32 v206, 1, v100
	v_lshlrev_b32_e32 v207, 1, v102
	v_mov_b32_e32 v158, v175
	v_mov_b32_e32 v159, v175
	v_mov_b32_e32 v160, v175
	v_mov_b32_e32 v161, v175
	v_mov_b32_e32 v154, v175
	v_mov_b32_e32 v155, v175
	v_mov_b32_e32 v156, v175
	v_mov_b32_e32 v157, v175
	v_mov_b32_e32 v150, v175
	v_mov_b32_e32 v151, v175
	v_mov_b32_e32 v152, v175
	v_mov_b32_e32 v153, v175
	v_mov_b32_e32 v106, v175
	v_mov_b32_e32 v107, v175
	v_mov_b32_e32 v108, v175
	v_mov_b32_e32 v109, v175

.LBB0_3617:
	s_or_b64 exec, exec, s[0:1]
	s_ashr_i32 s8, s8, 6
	s_and_b32 s0, s8, 3
	s_waitcnt vmcnt(0)
	v_and_b32_e32 v1, 63, v70
	s_cmp_gt_u32 s0, 1
	s_waitcnt lgkmcnt(0)
	s_barrier
	s_cbranch_scc1 .Lcv1_idle
	s_lshr_b32 s1, s96, 2
	s_and_b32 s1, s1, 2
	s_lshr_b32 s11, s96, 1
	s_and_b32 s11, s11, 0x38
	s_and_b32 s10, s96, 7
	s_or_b32 s11, s11, s10
	s_or_b32 s10, s0, s1
	s_lshl_b32 s1, s0, 14
	s_and_b32 s18, s11, 1
	s_add_i32 s19, s1, 0
	s_lshl_b32 s9, s0, 6
	s_mov_b32 s20, 0
	s_mov_b64 s[6:7], -1
	s_cmp_gt_i32 s8, 3
	v_cmp_eq_u32_e64 s[0:1], 0, v1
	s_cbranch_scc1 .LBB0_3663
	s_setprio 3
	s_lshl_b32 s21, s11, 7
	s_cmp_eq_u32 s18, 0
	s_cselect_b64 s[6:7], -1, 0
	s_and_b64 s[2:3], s[6:7], exec
	s_cselect_b32 s2, 0, 0x7f
	s_cselect_b32 s25, 1, 0x7e
	s_or_b32 s2, s2, s21
	s_add_u32 s22, s4, 0x4400000
	s_addc_u32 s23, s5, 0
	s_ashr_i32 s3, s2, 31
	s_lshl_b64 s[14:15], s[2:3], 13
	s_add_u32 s16, s22, s14
	s_addc_u32 s17, s23, s15
	s_add_u32 s12, s4, 0x8400000
	s_addc_u32 s13, s5, 0
	s_add_u32 s26, s12, s14
	v_mov_b32_e32 v187, 0
	s_addc_u32 s27, s13, s15
	v_lshlrev_b32_e32 v14, 4, v1
	v_mov_b32_e32 v15, v187
	s_add_u32 s14, s4, 0x3ea00000
	v_lshl_add_u64 v[2:3], s[16:17], 0, v[14:15]
	s_movk_i32 s24, 0x1000
	s_addc_u32 s15, s5, 0
	s_lshl_b64 s[2:3], s[2:3], 8
	v_add_co_u32_e32 v2, vcc, s24, v2
	s_add_u32 s2, s14, s2
	v_lshlrev_b32_e32 v188, 3, v1
	v_addc_co_u32_e32 v3, vcc, 0, v3, vcc
	s_addc_u32 s3, s15, s3
	v_and_b32_e32 v186, 48, v70
	global_load_dwordx4 v[42:45], v14, s[16:17]
	global_load_dwordx4 v[34:37], v14, s[16:17] offset:1024
	v_lshl_or_b32 v98, s10, 11, v188
	global_load_dwordx4 v[18:21], v14, s[16:17] offset:2048
	global_load_dwordx4 v[22:25], v14, s[16:17] offset:3072
	global_load_dwordx4 v[46:49], v186, s[2:3]
	global_load_dwordx4 v[26:29], v186, s[2:3] offset:64
	global_load_dwordx4 v[10:13], v[2:3], off offset:1024
	s_nop 0
	global_load_dwordx4 v[2:5], v[2:3], off offset:3072
	s_nop 0
	global_load_dwordx2 v[196:197], v98, s[26:27]
	global_load_dwordx2 v[184:185], v98, s[26:27] offset:512
	global_load_dwordx2 v[182:183], v98, s[26:27] offset:1024
	global_load_dwordx2 v[194:195], v98, s[26:27] offset:1536
	global_load_dwordx4 v[30:33], v186, s[2:3] offset:128
	global_load_dwordx4 v[6:9], v186, s[2:3] offset:192
	s_or_b32 s2, s25, s21
	s_ashr_i32 s3, s2, 31
	s_lshl_b64 s[26:27], s[2:3], 13
	s_add_u32 s28, s22, s26
	s_addc_u32 s29, s23, s27
	s_add_u32 s26, s12, s26
	v_or_b32_e32 v100, 0x800, v188
	s_addc_u32 s27, s13, s27
	s_lshl_b64 s[2:3], s[2:3], 8
	v_lshlrev_b32_e32 v50, 1, v100
	s_add_u32 s2, s14, s2
	v_lshl_add_u64 v[16:17], s[28:29], 0, v[14:15]
	v_or_b32_e32 v102, 0xc00, v188
	s_addc_u32 s3, s15, s3
	global_load_dwordx4 v[86:89], v14, s[28:29]
	global_load_dwordx4 v[78:81], v14, s[28:29] offset:1024
	global_load_dwordx4 v[62:65], v14, s[28:29] offset:2048
	global_load_dwordx4 v[66:69], v14, s[28:29] offset:3072
	global_load_dwordx4 v[94:97], v186, s[2:3]
	global_load_dwordx4 v[82:85], v186, s[2:3] offset:64
	global_load_dwordx4 v[38:41], v50, s[16:17]
	global_load_dwordx4 v[58:61], v50, s[28:29]
	v_add_co_u32_e32 v50, vcc, s24, v16
	v_lshlrev_b32_e32 v52, 1, v102
	s_nop 0
	v_addc_co_u32_e32 v51, vcc, 0, v17, vcc
	global_load_dwordx4 v[14:17], v52, s[16:17]
	global_load_dwordx4 v[54:57], v52, s[28:29]
	global_load_dwordx4 v[70:73], v[50:51], off offset:1024
	s_nop 0
	global_load_dwordx4 v[50:53], v[50:51], off offset:3072
	s_nop 0
	global_load_dwordx2 v[204:205], v98, s[26:27]
	global_load_dwordx2 v[202:203], v98, s[26:27] offset:512
	global_load_dwordx2 v[200:201], v98, s[26:27] offset:1024
	global_load_dwordx2 v[198:199], v98, s[26:27] offset:1536
	global_load_dwordx4 v[90:93], v186, s[2:3] offset:128
	global_load_dwordx4 v[74:77], v186, s[2:3] offset:192
	v_mov_b32_e32 v99, v187
	v_lshl_add_u64 v[190:191], s[14:15], 0, v[186:187]
	v_lshl_add_u64 v[192:193], s[12:13], 0, v[98:99]
	v_add_u32_e32 v189, s19, v188
	v_lshlrev_b32_e32 v220, 1, v100
	v_lshlrev_b32_e32 v221, 1, v102
	v_mov_b32_e32 v154, v187
	v_mov_b32_e32 v155, v187
	v_mov_b32_e32 v156, v187
	v_mov_b32_e32 v157, v187
	v_mov_b32_e32 v150, v187
	v_mov_b32_e32 v151, v187
	v_mov_b32_e32 v152, v187
	v_mov_b32_e32 v153, v187
	v_mov_b32_e32 v102, v187
	v_mov_b32_e32 v103, v187
	v_mov_b32_e32 v104, v187
	v_mov_b32_e32 v105, v187
	v_mov_b32_e32 v106, v187
	v_mov_b32_e32 v107, v187
	v_mov_b32_e32 v108, v187
	v_mov_b32_e32 v109, v187
